# K1 streaming loop hand-rewritten: lean row/col reductions, DPP row_bcast instead of bpermute, scalar diag lane select
# speedup vs baseline: 1.0698x; 1.0119x over previous
.Lk1_nozero:
	v_readfirstlane_b32 s15, v66
	s_mov_b64 s[18:19], 0x40000
.LBB0_8:
	v_add_u32_e32 v18, s13, v68
	buffer_load_dwordx4 v[26:29], v18, s[8:11], 0 offen sc0 nt
	buffer_load_dwordx4 v[34:37], v18, s[8:11], 0 offen offset:2048 sc0 nt
	buffer_load_dwordx4 v[10:13], v18, s[8:11], 0 offen offset:1024 sc0 nt
	buffer_load_dwordx4 v[14:17], v18, s[8:11], 0 offen offset:3072 sc0 nt
	v_add_u32_e32 v46, 0x1000, v18
	buffer_load_dwordx4 v[30:33], v46, s[8:11], 0 offen sc0 nt
	buffer_load_dwordx4 v[38:41], v46, s[8:11], 0 offen offset:2048 sc0 nt
	buffer_load_dwordx4 v[18:21], v46, s[8:11], 0 offen offset:1024 sc0 nt
	buffer_load_dwordx4 v[22:25], v46, s[8:11], 0 offen offset:3072 sc0 nt
	s_bitcmp1_b32 s15, 8
	s_cselect_b64 s[20:21], -1, 0
	s_lshr_b32 s16, s15, 2
	s_and_b32 s16, s16, 63
	s_lshl_b64 s[4:5], 1, s16
	s_waitcnt vmcnt(4)
	v_pk_add_f32 v[72:73], v[26:27], v[28:29]
	v_pk_add_f32 v[74:75], v[10:11], v[12:13]
	v_pk_add_f32 v[76:77], v[34:35], v[36:37]
	v_pk_add_f32 v[78:79], v[14:15], v[16:17]
	v_pk_add_f32 v[58:59], v[26:27], v[34:35]
	v_pk_add_f32 v[60:61], v[28:29], v[36:37]
	v_pk_add_f32 v[72:73], v[72:73], v[74:75]
	v_pk_add_f32 v[76:77], v[76:77], v[78:79]
	v_pk_add_f32 v[54:55], v[10:11], v[14:15]
	v_pk_add_f32 v[56:57], v[12:13], v[16:17]
	v_add_f32_e32 v50, v72, v73
	v_add_f32_e32 v51, v76, v77
	s_waitcnt vmcnt(0)
	v_pk_add_f32 v[72:73], v[30:31], v[32:33]
	v_pk_add_f32 v[74:75], v[18:19], v[20:21]
	v_pk_add_f32 v[76:77], v[38:39], v[40:41]
	v_pk_add_f32 v[78:79], v[22:23], v[24:25]
	v_pk_add_f32 v[46:47], v[30:31], v[38:39]
	v_pk_add_f32 v[48:49], v[32:33], v[40:41]
	v_pk_add_f32 v[72:73], v[72:73], v[74:75]
	v_pk_add_f32 v[76:77], v[76:77], v[78:79]
	v_pk_add_f32 v[58:59], v[58:59], v[46:47]
	v_pk_add_f32 v[60:61], v[60:61], v[48:49]
	v_pk_add_f32 v[46:47], v[18:19], v[22:23]
	v_pk_add_f32 v[48:49], v[20:21], v[24:25]
	v_add_f32_e32 v52, v72, v73
	v_add_f32_e32 v53, v76, v77
	v_pk_add_f32 v[2:3], v[2:3], v[58:59]
	v_pk_add_f32 v[4:5], v[4:5], v[60:61]
	v_pk_add_f32 v[54:55], v[54:55], v[46:47]
	v_pk_add_f32 v[56:57], v[56:57], v[48:49]
	v_add_f32_e32 v70, v50, v51
	v_add_f32_e32 v71, v52, v53
	v_pk_add_f32 v[6:7], v[6:7], v[54:55]
	v_pk_add_f32 v[8:9], v[8:9], v[56:57]
	v_add_f32_e32 v70, v70, v71
	v_add_f32_e32 v43, v43, v70
	v_add_f32_dpp v50, v50, v50 quad_perm:[1,0,3,2] row_mask:0xf bank_mask:0xf
	v_add_f32_dpp v51, v51, v51 quad_perm:[1,0,3,2] row_mask:0xf bank_mask:0xf
	v_add_f32_dpp v52, v52, v52 quad_perm:[1,0,3,2] row_mask:0xf bank_mask:0xf
	v_add_f32_dpp v53, v53, v53 quad_perm:[1,0,3,2] row_mask:0xf bank_mask:0xf
	v_add_f32_dpp v50, v50, v50 quad_perm:[2,3,0,1] row_mask:0xf bank_mask:0xf
	v_add_f32_dpp v51, v51, v51 quad_perm:[2,3,0,1] row_mask:0xf bank_mask:0xf
	v_add_f32_dpp v52, v52, v52 quad_perm:[2,3,0,1] row_mask:0xf bank_mask:0xf
	v_add_f32_dpp v53, v53, v53 quad_perm:[2,3,0,1] row_mask:0xf bank_mask:0xf
	v_add_f32_dpp v50, v50, v50 row_half_mirror row_mask:0xf bank_mask:0xf
	v_add_f32_dpp v51, v51, v51 row_half_mirror row_mask:0xf bank_mask:0xf
	v_add_f32_dpp v52, v52, v52 row_half_mirror row_mask:0xf bank_mask:0xf
	v_add_f32_dpp v53, v53, v53 row_half_mirror row_mask:0xf bank_mask:0xf
	v_add_f32_dpp v50, v50, v50 row_mirror row_mask:0xf bank_mask:0xf
	v_add_f32_dpp v51, v51, v51 row_mirror row_mask:0xf bank_mask:0xf
	v_add_f32_dpp v52, v52, v52 row_mirror row_mask:0xf bank_mask:0xf
	v_add_f32_dpp v53, v53, v53 row_mirror row_mask:0xf bank_mask:0xf
	v_add_f32_dpp v50, v50, v50 row_bcast:15 row_mask:0xa bank_mask:0xf
	v_add_f32_dpp v51, v51, v51 row_bcast:15 row_mask:0xa bank_mask:0xf
	v_add_f32_dpp v52, v52, v52 row_bcast:15 row_mask:0xa bank_mask:0xf
	v_add_f32_dpp v53, v53, v53 row_bcast:15 row_mask:0xa bank_mask:0xf
	v_add_f32_dpp v50, v50, v50 row_bcast:31 row_mask:0xc bank_mask:0xf
	v_add_f32_dpp v51, v51, v51 row_bcast:31 row_mask:0xc bank_mask:0xf
	v_add_f32_dpp v52, v52, v52 row_bcast:31 row_mask:0xc bank_mask:0xf
	v_add_f32_dpp v53, v53, v53 row_bcast:31 row_mask:0xc bank_mask:0xf
	s_mov_b64 exec, s[4:5]
	v_cndmask_b32_e64 v58, v26, v10, s[20:21]
	v_cndmask_b32_e64 v59, v35, v15, s[20:21]
	v_cndmask_b32_e64 v60, v32, v20, s[20:21]
	v_cndmask_b32_e64 v61, v41, v25, s[20:21]
	global_store_dwordx4 v[44:45], v[58:61], off
	v_add_f32_e32 v70, v58, v59
	v_add_f32_e32 v71, v60, v61
	v_add_f32_e32 v70, v70, v71
	v_add_f32_e32 v42, v42, v70
	s_mov_b32 s4, 0
	s_brev_b32 s5, 1
	s_mov_b64 exec, s[4:5]
	v_lshl_add_u64 v[70:71], v[44:45], 0, s[18:19]
	global_store_dwordx4 v[70:71], v[50:53], off
	s_mov_b64 exec, -1
	s_add_i32 s13, s13, 0x8000
	s_add_u32 s15, s15, 16
	v_lshl_add_u64 v[44:45], v[44:45], 0, 64
	s_cmp_eq_u32 s13, 0x20000
	s_cbranch_scc0 .LBB0_8

	.amdhsa_kernel _Z9k1_streamPKfPf6PfArgs
		.amdhsa_group_segment_fixed_size 8224
		.amdhsa_private_segment_fixed_size 0
		.amdhsa_kernarg_size 80
		.amdhsa_user_sgpr_count 2
		.amdhsa_user_sgpr_dispatch_ptr 0
		.amdhsa_user_sgpr_queue_ptr 0
		.amdhsa_user_sgpr_kernarg_segment_ptr 1
		.amdhsa_user_sgpr_dispatch_id 0
		.amdhsa_user_sgpr_kernarg_preload_length 0
		.amdhsa_user_sgpr_kernarg_preload_offset 0
		.amdhsa_user_sgpr_private_segment_size 0
		.amdhsa_uses_dynamic_stack 0
		.amdhsa_enable_private_segment 0
		.amdhsa_system_sgpr_workgroup_id_x 1
		.amdhsa_system_sgpr_workgroup_id_y 0
		.amdhsa_system_sgpr_workgroup_id_z 0
		.amdhsa_system_sgpr_workgroup_info 0
		.amdhsa_system_vgpr_workitem_id 0
		.amdhsa_next_free_vgpr 80
		.amdhsa_next_free_sgpr 22
		.amdhsa_accum_offset 80
		.amdhsa_reserve_vcc 1
		.amdhsa_float_round_mode_32 0
		.amdhsa_float_round_mode_16_64 0
		.amdhsa_float_denorm_mode_32 3
		.amdhsa_float_denorm_mode_16_64 3
		.amdhsa_dx10_clamp 1
		.amdhsa_ieee_mode 1
		.amdhsa_fp16_overflow 0
		.amdhsa_tg_split 0
		.amdhsa_exception_fp_ieee_invalid_op 0
		.amdhsa_exception_fp_denorm_src 0
		.amdhsa_exception_fp_ieee_div_zero 0
		.amdhsa_exception_fp_ieee_overflow 0
		.amdhsa_exception_fp_ieee_underflow 0
		.amdhsa_exception_fp_ieee_inexact 0
		.amdhsa_exception_int_div_zero 0
	.end_amdhsa_kernel

amdhsa.kernels:
  - .agpr_count:     0
    .args:
      - .actual_access:  read_only
        .address_space:  global
        .offset:         0
        .size:           8
        .value_kind:     global_buffer
      - .actual_access:  write_only
        .address_space:  global
        .offset:         8
        .size:           8
        .value_kind:     global_buffer
      - .offset:         16
        .size:           64
        .value_kind:     by_value
    .group_segment_fixed_size: 8224
    .kernarg_segment_align: 8
    .kernarg_segment_size: 80
    .language:       OpenCL C
    .language_version:
      - 2
      - 0
    .max_flat_workgroup_size: 256
    .name:           _Z9k1_streamPKfPf6PfArgs
    .private_segment_fixed_size: 0
    .sgpr_count:     28
    .sgpr_spill_count: 0
    .symbol:         _Z9k1_streamPKfPf6PfArgs.kd
    .uniform_work_group_size: 1
    .uses_dynamic_stack: false
    .vgpr_count:     80
    .vgpr_spill_count: 0
    .wavefront_size: 64
  - .agpr_count:     0
    .args:
      - .actual_access:  read_only
        .address_space:  global
        .offset:         0
        .size:           8
        .value_kind:     global_buffer
      - .actual_access:  read_only
        .address_space:  global
        .offset:         8
        .size:           8
        .value_kind:     global_buffer
      - .actual_access:  read_only
        .address_space:  global
        .offset:         16
        .size:           8
        .value_kind:     global_buffer
      - .actual_access:  write_only
        .address_space:  global
        .offset:         24
        .size:           8
        .value_kind:     global_buffer
      - .address_space:  global
        .offset:         32
        .size:           8
        .value_kind:     global_buffer
      - .address_space:  global
        .offset:         40
        .size:           8
        .value_kind:     global_buffer
    .group_segment_fixed_size: 3712
    .kernarg_segment_align: 8
    .kernarg_segment_size: 48
    .language:       OpenCL C
    .language_version:
      - 2
      - 0
    .max_flat_workgroup_size: 256
    .name:           _Z9k2_layer1PKfS0_S0_PfS1_S1_
    .private_segment_fixed_size: 0
    .sgpr_count:     32
    .sgpr_spill_count: 0
    .symbol:         _Z9k2_layer1PKfS0_S0_PfS1_S1_.kd
    .uniform_work_group_size: 1
    .uses_dynamic_stack: false
    .vgpr_count:     92
    .vgpr_spill_count: 0
    .wavefront_size: 64
  - .agpr_count:     8
    .args:
      - .actual_access:  read_only
        .address_space:  global
        .offset:         0
        .size:           8
        .value_kind:     global_buffer
      - .actual_access:  read_only
        .address_space:  global
        .offset:         8
        .size:           8
        .value_kind:     global_buffer
      - .actual_access:  read_only
        .address_space:  global
        .offset:         16
        .size:           8
        .value_kind:     global_buffer
      - .actual_access:  read_only
        .address_space:  global
        .offset:         24
        .size:           8
        .value_kind:     global_buffer
      - .actual_access:  read_only
        .address_space:  global
        .offset:         32
        .size:           8
        .value_kind:     global_buffer
      - .actual_access:  read_only
        .address_space:  global
        .offset:         40
        .size:           8
        .value_kind:     global_buffer
      - .actual_access:  read_only
        .address_space:  global
        .offset:         48
        .size:           8
        .value_kind:     global_buffer
      - .actual_access:  write_only
        .address_space:  global
        .offset:         56
        .size:           8
        .value_kind:     global_buffer
      - .address_space:  global
        .offset:         64
        .size:           8
        .value_kind:     global_buffer
      - .address_space:  global
        .offset:         72
        .size:           8
        .value_kind:     global_buffer
    .group_segment_fixed_size: 1280
    .kernarg_segment_align: 8
    .kernarg_segment_size: 80
    .language:       OpenCL C
    .language_version:
      - 2
      - 0
    .max_flat_workgroup_size: 256
    .name:           _Z7k_layerPKfS0_S0_S0_S0_S0_S0_PfS1_S1_
    .private_segment_fixed_size: 0
    .sgpr_count:     40
    .sgpr_spill_count: 0
    .symbol:         _Z7k_layerPKfS0_S0_S0_S0_S0_S0_PfS1_S1_.kd
    .uniform_work_group_size: 1
    .uses_dynamic_stack: false
    .vgpr_count:     104
    .vgpr_spill_count: 0
    .wavefront_size: 64
  - .agpr_count:     12
    .args:
      - .actual_access:  read_only
        .address_space:  global
        .offset:         0
        .size:           8
        .value_kind:     global_buffer
      - .actual_access:  read_only
        .address_space:  global
        .offset:         8
        .size:           8
        .value_kind:     global_buffer
      - .actual_access:  read_only
        .address_space:  global
        .offset:         16
        .size:           8
        .value_kind:     global_buffer
      - .actual_access:  read_only
        .address_space:  global
        .offset:         24
        .size:           8
        .value_kind:     global_buffer
      - .actual_access:  read_only
        .address_space:  global
        .offset:         32
        .size:           8
        .value_kind:     global_buffer
      - .actual_access:  read_only
        .address_space:  global
        .offset:         40
        .size:           8
        .value_kind:     global_buffer
      - .actual_access:  read_only
        .address_space:  global
        .offset:         48
        .size:           8
        .value_kind:     global_buffer
      - .actual_access:  read_only
        .address_space:  global
        .offset:         56
        .size:           8
        .value_kind:     global_buffer
      - .actual_access:  read_only
        .address_space:  global
        .offset:         64
        .size:           8
        .value_kind:     global_buffer
      - .actual_access:  write_only
        .address_space:  global
        .offset:         72
        .size:           8
        .value_kind:     global_buffer
    .group_segment_fixed_size: 4608
    .kernarg_segment_align: 8
    .kernarg_segment_size: 80
    .language:       OpenCL C
    .language_version:
      - 2
      - 0
    .max_flat_workgroup_size: 256
    .name:           _Z8k5_finalPKfS0_S0_S0_S0_S0_S0_S0_S0_Pf
    .private_segment_fixed_size: 0
    .sgpr_count:     30
    .sgpr_spill_count: 0
    .symbol:         _Z8k5_finalPKfS0_S0_S0_S0_S0_S0_S0_S0_Pf.kd
    .uniform_work_group_size: 1
    .uses_dynamic_stack: false
    .vgpr_count:     96
    .vgpr_spill_count: 0
    .wavefront_size: 64
